# nt hint also on the P3 epilogue's streaming read-once residual x loads
# speedup vs baseline: 1.0378x; 1.0061x over previous
.LBB0_1451:
	s_lshl_b32 s0, s7, 5
	s_lshl_b32 s1, s8, 8
	s_or_b32 s0, s1, s0
	s_lshl_b32 s18, s6, 8
	v_and_or_b32 v200, v146, 12, s0
	s_add_i32 s0, s18, s36
	v_or_b32_e32 v194, s0, v1
	v_ashrrev_i32_e32 v201, 31, v200
	v_ashrrev_i32_e32 v195, 31, v194
	v_lshl_add_u64 v[202:203], v[200:201], 2, s[52:53]
	v_lshlrev_b64 v[130:131], 12, v[194:195]
	v_or_b32_e32 v146, 16, v194
	v_or_b32_e32 v158, 32, v194
	v_or_b32_e32 v174, 48, v194
	v_lshl_add_u64 v[130:131], v[202:203], 0, v[130:131]
	v_ashrrev_i32_e32 v147, 31, v146
	v_ashrrev_i32_e32 v159, 31, v158
	v_ashrrev_i32_e32 v175, 31, v174
	s_barrier
	global_load_dwordx4 v[142:145], v[130:131], off nt
	global_load_dwordx4 v[138:141], v[130:131], off offset:64 nt
	global_load_dwordx4 v[134:137], v[130:131], off offset:512 nt
	s_nop 0
	global_load_dwordx4 v[130:133], v[130:131], off offset:576 nt
	v_lshlrev_b64 v[146:147], 12, v[146:147]
	v_lshlrev_b64 v[158:159], 12, v[158:159]
	v_lshlrev_b64 v[174:175], 12, v[174:175]
	v_lshl_add_u64 v[146:147], v[202:203], 0, v[146:147]
	v_lshl_add_u64 v[158:159], v[202:203], 0, v[158:159]
	v_lshl_add_u64 v[174:175], v[202:203], 0, v[174:175]
	global_load_dwordx4 v[162:165], v[146:147], off nt
	global_load_dwordx4 v[154:157], v[146:147], off offset:64 nt
	global_load_dwordx4 v[150:153], v[146:147], off offset:512 nt
	s_nop 0
	global_load_dwordx4 v[146:149], v[146:147], off offset:576 nt
	s_nop 0
	global_load_dwordx4 v[178:181], v[158:159], off nt
	global_load_dwordx4 v[170:173], v[158:159], off offset:64 nt
	global_load_dwordx4 v[166:169], v[158:159], off offset:512 nt
	s_nop 0
	global_load_dwordx4 v[158:161], v[158:159], off offset:576 nt
	s_nop 0
	global_load_dwordx4 v[190:193], v[174:175], off nt
	global_load_dwordx4 v[186:189], v[174:175], off offset:64 nt
	global_load_dwordx4 v[182:185], v[174:175], off offset:512 nt
	s_nop 0
	global_load_dwordx4 v[174:177], v[174:175], off offset:576 nt
	s_mov_b32 s0, 0x3f9837f0
	v_add_u32_e32 v196, 0x80, v194
	v_ashrrev_i32_e32 v197, 31, v196
	v_lshlrev_b64 v[196:197], 12, v[196:197]
	v_lshl_add_u64 v[196:197], v[202:203], 0, v[196:197]
	s_waitcnt vmcnt(0)
	v_pk_fma_f32 v[144:145], v[144:145], s[0:1], v[128:129] op_sel_hi:[1,0,1]
	v_pk_fma_f32 v[142:143], v[142:143], s[0:1], v[126:127] op_sel_hi:[1,0,1]
	v_pk_fma_f32 v[140:141], v[140:141], s[0:1], v[124:125] op_sel_hi:[1,0,1]
	v_pk_fma_f32 v[130:131], v[130:131], s[0:1], v[94:95] op_sel_hi:[1,0,1]
	v_pk_fma_f32 v[132:133], v[132:133], s[0:1], v[96:97] op_sel_hi:[1,0,1]
	v_pk_fma_f32 v[138:139], v[138:139], s[0:1], v[122:123] op_sel_hi:[1,0,1]
	v_pk_fma_f32 v[136:137], v[136:137], s[0:1], v[104:105] op_sel_hi:[1,0,1]
	v_pk_fma_f32 v[134:135], v[134:135], s[0:1], v[102:103] op_sel_hi:[1,0,1]
	v_pk_fma_f32 v[128:129], v[164:165], s[0:1], v[120:121] op_sel_hi:[1,0,1]
	v_pk_fma_f32 v[94:95], v[170:171], s[0:1], v[106:107] op_sel_hi:[1,0,1]
	v_add_u32_e32 v106, 0x90, v194
	v_pk_fma_f32 v[96:97], v[172:173], s[0:1], v[108:109] op_sel_hi:[1,0,1]
	v_ashrrev_i32_e32 v107, 31, v106
	v_add_u32_e32 v108, 0xa0, v194
	v_pk_fma_f32 v[126:127], v[162:163], s[0:1], v[118:119] op_sel_hi:[1,0,1]
	v_pk_fma_f32 v[124:125], v[156:157], s[0:1], v[116:117] op_sel_hi:[1,0,1]
	v_pk_fma_f32 v[122:123], v[154:155], s[0:1], v[114:115] op_sel_hi:[1,0,1]
	v_pk_fma_f32 v[120:121], v[152:153], s[0:1], v[88:89] op_sel_hi:[1,0,1]
	v_pk_fma_f32 v[118:119], v[150:151], s[0:1], v[86:87] op_sel_hi:[1,0,1]
	v_pk_fma_f32 v[116:117], v[148:149], s[0:1], v[84:85] op_sel_hi:[1,0,1]
	v_pk_fma_f32 v[114:115], v[146:147], s[0:1], v[82:83] op_sel_hi:[1,0,1]
	v_pk_fma_f32 v[104:105], v[180:181], s[0:1], v[112:113] op_sel_hi:[1,0,1]
	v_pk_fma_f32 v[102:103], v[178:179], s[0:1], v[110:111] op_sel_hi:[1,0,1]
	v_pk_fma_f32 v[88:89], v[168:169], s[0:1], v[80:81] op_sel_hi:[1,0,1]
	v_pk_fma_f32 v[86:87], v[166:167], s[0:1], v[78:79] op_sel_hi:[1,0,1]
	v_pk_fma_f32 v[84:85], v[160:161], s[0:1], v[76:77] op_sel_hi:[1,0,1]
	v_pk_fma_f32 v[82:83], v[158:159], s[0:1], v[74:75] op_sel_hi:[1,0,1]
	v_pk_fma_f32 v[80:81], v[192:193], s[0:1], v[100:101] op_sel_hi:[1,0,1]
	v_pk_fma_f32 v[78:79], v[190:191], s[0:1], v[98:99] op_sel_hi:[1,0,1]
	v_pk_fma_f32 v[76:77], v[188:189], s[0:1], v[92:93] op_sel_hi:[1,0,1]
	v_pk_fma_f32 v[74:75], v[186:187], s[0:1], v[90:91] op_sel_hi:[1,0,1]
	v_pk_fma_f32 v[72:73], v[184:185], s[0:1], v[72:73] op_sel_hi:[1,0,1]
	v_pk_fma_f32 v[70:71], v[182:183], s[0:1], v[70:71] op_sel_hi:[1,0,1]
	v_pk_fma_f32 v[68:69], v[176:177], s[0:1], v[68:69] op_sel_hi:[1,0,1]
	v_pk_fma_f32 v[66:67], v[174:175], s[0:1], v[66:67] op_sel_hi:[1,0,1]
	v_lshlrev_b64 v[106:107], 12, v[106:107]
	v_ashrrev_i32_e32 v109, 31, v108
	v_lshl_add_u64 v[106:107], v[202:203], 0, v[106:107]
	v_lshlrev_b64 v[108:109], 12, v[108:109]
	global_load_dwordx4 v[166:169], v[106:107], off nt
	global_load_dwordx4 v[170:173], v[106:107], off offset:64 nt
	global_load_dwordx4 v[174:177], v[106:107], off offset:512 nt
	global_load_dwordx4 v[178:181], v[106:107], off offset:576 nt
	v_lshl_add_u64 v[106:107], v[202:203], 0, v[108:109]
	global_load_dwordx4 v[90:93], v[196:197], off nt
	global_load_dwordx4 v[98:101], v[196:197], off offset:64 nt
	global_load_dwordx4 v[150:153], v[196:197], off offset:512 nt
	global_load_dwordx4 v[162:165], v[196:197], off offset:576 nt
	v_add_u32_e32 v108, 0xb0, v194
	global_load_dwordx4 v[190:193], v[106:107], off offset:512 nt
	global_load_dwordx4 v[194:197], v[106:107], off offset:576 nt
	v_ashrrev_i32_e32 v109, 31, v108
	v_lshlrev_b64 v[108:109], 12, v[108:109]
	global_load_dwordx4 v[182:185], v[106:107], off nt
	global_load_dwordx4 v[186:189], v[106:107], off offset:64 nt
	v_lshl_add_u64 v[106:107], v[202:203], 0, v[108:109]
	global_load_dwordx4 v[158:161], v[106:107], off nt
	global_load_dwordx4 v[154:157], v[106:107], off offset:64 nt
	global_load_dwordx4 v[146:149], v[106:107], off offset:512 nt
	global_load_dwordx4 v[210:213], v[106:107], off offset:576 nt
	v_mbcnt_lo_u32_b32 v108, -1, 0
	v_mbcnt_hi_u32_b32 v203, -1, v108
	v_and_b32_e32 v109, 64, v203
	v_xor_b32_e32 v108, 16, v203
	v_add_u32_e32 v209, 64, v109
	v_cmp_lt_i32_e32 vcc, v108, v209
	v_mov_b32_e32 v109, v144
	v_mov_b32_e32 v110, v142
	v_cndmask_b32_e32 v108, v203, v108, vcc
	v_lshlrev_b32_e32 v202, 2, v108
	v_mov_b32_e32 v108, v143
	v_mov_b32_e32 v111, v145
	v_mov_b32_e32 v112, v139
	v_mov_b32_e32 v113, v140
	v_mov_b32_e32 v214, v138
	v_mov_b32_e32 v215, v141
	v_pk_add_f32 v[106:107], v[108:109], v[110:111]
	v_pk_add_f32 v[108:109], v[112:113], v[214:215]
	v_add_f32_e32 v112, v106, v107
	v_pk_add_f32 v[106:107], v[108:109], v[108:109] op_sel_hi:[0,1]
	v_add_f32_e32 v217, v134, v135
	v_add_f32_e32 v219, v136, v137
	v_mov_b32_e32 v216, v130
	v_mov_b32_e32 v218, v131
	v_mov_b32_e32 v220, v133
	v_add_f32_e32 v221, 0, v112
	v_mov_b32_e32 v106, v132
	v_pk_add_f32 v[110:111], v[216:217], v[218:219]
	v_pk_add_f32 v[106:107], v[106:107], v[220:221]
	s_waitcnt vmcnt(11)
	v_pk_fma_f32 v[112:113], v[92:93], s[0:1], v[64:65] op_sel_hi:[1,0,1]
	v_pk_add_f32 v[214:215], v[110:111], v[106:107]
	s_waitcnt vmcnt(10)
	v_pk_fma_f32 v[106:107], v[98:99], s[0:1], v[58:59] op_sel_hi:[1,0,1]
	v_pk_fma_f32 v[58:59], v[170:171], s[0:1], v[50:51] op_sel_hi:[1,0,1]
	v_pk_fma_f32 v[50:51], v[178:179], s[0:1], v[18:19] op_sel_hi:[1,0,1]
	v_pk_fma_f32 v[108:109], v[100:101], s[0:1], v[60:61] op_sel_hi:[1,0,1]
	s_waitcnt vmcnt(6)
	v_pk_fma_f32 v[18:19], v[194:195], s[0:1], v[10:11] op_sel_hi:[1,0,1]
	v_add_f32_e32 v10, v214, v215
	ds_bpermute_b32 v11, v202, v10
	v_pk_fma_f32 v[60:61], v[172:173], s[0:1], v[52:53] op_sel_hi:[1,0,1]
	v_pk_fma_f32 v[52:53], v[180:181], s[0:1], v[20:21] op_sel_hi:[1,0,1]
	v_pk_fma_f32 v[20:21], v[196:197], s[0:1], v[12:13] op_sel_hi:[1,0,1]
	v_xor_b32_e32 v12, 32, v203
	v_cmp_lt_i32_e32 vcc, v12, v209
	v_pk_fma_f32 v[64:65], v[168:169], s[0:1], v[56:57] op_sel_hi:[1,0,1]
	v_pk_fma_f32 v[56:57], v[176:177], s[0:1], v[28:29] op_sel_hi:[1,0,1]
	v_cndmask_b32_e32 v12, v203, v12, vcc
	v_pk_fma_f32 v[28:29], v[192:193], s[0:1], v[16:17] op_sel_hi:[1,0,1]
	s_waitcnt vmcnt(3)
	v_pk_fma_f32 v[16:17], v[160:161], s[0:1], v[32:33] op_sel_hi:[1,0,1]
	v_lshlrev_b32_e32 v32, 2, v12
	s_waitcnt lgkmcnt(0)
	v_add_f32_e32 v33, v10, v11
	v_pk_fma_f32 v[110:111], v[90:91], s[0:1], v[62:63] op_sel_hi:[1,0,1]
	v_pk_fma_f32 v[90:91], v[162:163], s[0:1], v[34:35] op_sel_hi:[1,0,1]
	v_pk_fma_f32 v[34:35], v[186:187], s[0:1], v[42:43] op_sel_hi:[1,0,1]
	ds_bpermute_b32 v42, v32, v33
	s_waitcnt vmcnt(2)
	v_pk_fma_f32 v[10:11], v[154:155], s[0:1], v[22:23] op_sel_hi:[1,0,1]
	v_pk_fma_f32 v[62:63], v[166:167], s[0:1], v[54:55] op_sel_hi:[1,0,1]
	v_pk_fma_f32 v[54:55], v[174:175], s[0:1], v[26:27] op_sel_hi:[1,0,1]
	v_pk_fma_f32 v[26:27], v[190:191], s[0:1], v[14:15] op_sel_hi:[1,0,1]
	s_waitcnt lgkmcnt(0)
	v_add_f32_e32 v22, v33, v42
	v_pk_fma_f32 v[14:15], v[158:159], s[0:1], v[30:31] op_sel_hi:[1,0,1]
	v_pk_fma_f32 v[12:13], v[156:157], s[0:1], v[24:25] op_sel_hi:[1,0,1]
	v_fmamk_f32 v24, v22, 0xbc800000, v145
	v_fmamk_f32 v30, v22, 0xbc800000, v143
	v_fmamk_f32 v23, v22, 0xbc800000, v144
	v_fmamk_f32 v25, v22, 0xbc800000, v142
	v_mul_f32_e32 v30, v30, v30
	v_mul_f32_e32 v24, v24, v24
	v_fmac_f32_e32 v30, v25, v25
	v_fmac_f32_e32 v24, v23, v23
	v_fmamk_f32 v25, v22, 0xbc800000, v141
	v_fmamk_f32 v31, v22, 0xbc800000, v139
	v_add_f32_e32 v23, v30, v24
	v_fmamk_f32 v24, v22, 0xbc800000, v140
	v_fmamk_f32 v30, v22, 0xbc800000, v138
	v_mul_f32_e32 v31, v31, v31
	v_mul_f32_e32 v25, v25, v25
	v_fmac_f32_e32 v31, v30, v30
	v_fmac_f32_e32 v25, v24, v24
	v_add_f32_e32 v24, v31, v25
	v_fmamk_f32 v25, v22, 0xbc800000, v137
	v_fmamk_f32 v31, v22, 0xbc800000, v135
	v_add_f32_e32 v23, v23, v24
	v_fmamk_f32 v24, v22, 0xbc800000, v136
	v_fmamk_f32 v30, v22, 0xbc800000, v134
	v_mul_f32_e32 v31, v31, v31
	v_mul_f32_e32 v25, v25, v25
	v_fmac_f32_e32 v31, v30, v30
	v_fmac_f32_e32 v25, v24, v24
	v_add_f32_e32 v24, v31, v25
	v_fmamk_f32 v25, v22, 0xbc800000, v133
	v_fmamk_f32 v31, v22, 0xbc800000, v131
	v_add_f32_e32 v23, v24, v23
	v_fmamk_f32 v24, v22, 0xbc800000, v132
	v_fmamk_f32 v30, v22, 0xbc800000, v130
	v_mul_f32_e32 v31, v31, v31
	v_mul_f32_e32 v25, v25, v25
	v_fmac_f32_e32 v31, v30, v30
	v_fmac_f32_e32 v25, v24, v24
	v_add_f32_e32 v24, v31, v25
	v_add_f32_e32 v23, v24, v23
	ds_bpermute_b32 v24, v202, v23
	v_pk_fma_f32 v[100:101], v[152:153], s[0:1], v[40:41] op_sel_hi:[1,0,1]
	v_pk_fma_f32 v[98:99], v[150:151], s[0:1], v[38:39] op_sel_hi:[1,0,1]
	v_pk_fma_f32 v[92:93], v[164:165], s[0:1], v[36:37] op_sel_hi:[1,0,1]
	v_pk_fma_f32 v[40:41], v[184:185], s[0:1], v[48:49] op_sel_hi:[1,0,1]
	s_waitcnt lgkmcnt(0)
	v_add_f32_e32 v23, v23, v24
	ds_bpermute_b32 v24, v32, v23
	v_pk_fma_f32 v[38:39], v[182:183], s[0:1], v[46:47] op_sel_hi:[1,0,1]
	v_pk_fma_f32 v[36:37], v[188:189], s[0:1], v[44:45] op_sel_hi:[1,0,1]
	s_waitcnt vmcnt(1)
	v_pk_fma_f32 v[8:9], v[148:149], s[0:1], v[8:9] op_sel_hi:[1,0,1]
	v_pk_fma_f32 v[6:7], v[146:147], s[0:1], v[6:7] op_sel_hi:[1,0,1]
	s_waitcnt vmcnt(0)
	v_pk_fma_f32 v[4:5], v[212:213], s[0:1], v[4:5] op_sel_hi:[1,0,1]
	v_pk_fma_f32 v[2:3], v[210:211], s[0:1], v[2:3] op_sel_hi:[1,0,1]
	s_lshl_b32 s0, s7, 3
	v_cmp_gt_u32_e32 vcc, 16, v198
	s_add_i32 s2, s0, 0
	s_and_saveexec_b64 s[0:1], vcc
	s_cbranch_execz .LBB0_1453
	s_lshl_b32 s4, s9, 11
	s_add_i32 s4, s2, s4
	v_mul_f32_e32 v22, 0x3c800000, v22
	v_lshl_add_u32 v25, v1, 5, s4
	s_waitcnt lgkmcnt(0)
	v_add_f32_e32 v23, v23, v24
	ds_write_b64 v25, v[22:23]
